# nt (streaming) cache policy on the read-once f32 loads of the weight and activation conversions (P0, P4/P6-hosted)
# speedup vs baseline: 1.0076x; 1.0076x over previous
; #define GAS __attribute__((address_space(1)))
; template <bool UNCOND> DI void witem_load(const WItem& d, WRegs& R, int lane) {
;     const int n4 = lane & 31, kh = lane >> 5;
;     const float* src = d.W + (size_t)(d.k0 + 2 * kh) * d.N + d.src_col0 + 4 * n4;
; #pragma unroll
;     for (int i = 0; i < 8; ++i) { R.a[i] = *(const GAS f32x4*)(src + (size_t)(4 * i) * d.N); R.b[i] = *(const GAS f32x4*)(src + (size_t)(4 * i + 1) * d.N); }
;     if (UNCOND) {
;         const float* gp = d.gain ? d.gain + d.k0 + 2 * kh : src;
; #pragma unroll
;         for (int i = 0; i < 8; ++i) R.gg[i] = *(const GAS f32x2g*)(gp + 4 * i);
;         if (!d.gain) {
; #pragma unroll
;             for (int i = 0; i < 8; ++i) R.gg[i] = (f32x2g){1.f, 1.f}; }
;     } else if (d.gain) {
; #pragma unroll
;         for (int i = 0; i < 8; ++i) R.gg[i] = *(const GAS f32x2g*)(d.gain + d.k0 + 4 * i + 2 * kh); }
;     ...
;     if (v0) witem_load<PIPE>(d0, R0, lane);
.LBB0_32:
	v_lshrrev_b32_e32 v2, 4, v0
	v_and_b32_e32 v66, 2, v2
	v_add_u32_e32 v4, s14, v66
	s_mov_b32 s4, 0xe000
	s_waitcnt lgkmcnt(0)
	v_mov_b64_e32 v[2:3], s[42:43]
	v_mad_i64_i32 v[2:3], s[0:1], v4, s4, v[2:3]
	s_ashr_i32 s13, s12, 31
	v_lshlrev_b32_e32 v4, 4, v0
	v_lshl_add_u64 v[2:3], s[12:13], 2, v[2:3]
	v_and_b32_e32 v4, 0x1f0, v4
	v_mov_b32_e32 v5, 0
	v_lshl_add_u64 v[58:59], v[2:3], 0, v[4:5]
	v_add_co_u32_e32 v2, vcc, s4, v58
	s_mov_b32 s0, 0x38000
	s_nop 0
	v_addc_co_u32_e32 v3, vcc, 0, v59, vcc
	v_add_co_u32_e32 v10, vcc, s0, v58
	s_mov_b32 s0, 0x46000
	s_nop 0
	v_addc_co_u32_e32 v11, vcc, 0, v59, vcc
	v_add_co_u32_e32 v12, vcc, s0, v58
	s_mov_b32 s0, 0x70000
	s_nop 0
	v_addc_co_u32_e32 v13, vcc, 0, v59, vcc
	v_add_co_u32_e32 v18, vcc, s0, v58
	s_mov_b32 s0, 0x7e000
	s_nop 0
	v_addc_co_u32_e32 v19, vcc, 0, v59, vcc
	v_add_co_u32_e32 v20, vcc, s0, v58
	s_mov_b32 s0, 0xa8000
	s_nop 0
	v_addc_co_u32_e32 v21, vcc, 0, v59, vcc
	v_add_co_u32_e32 v26, vcc, s0, v58
	s_mov_b32 s0, 0xb6000
	s_nop 0
	v_addc_co_u32_e32 v27, vcc, 0, v59, vcc
	v_add_co_u32_e32 v28, vcc, s0, v58
	s_mov_b32 s0, 0xe0000
	s_nop 0
	v_addc_co_u32_e32 v29, vcc, 0, v59, vcc
	v_add_co_u32_e32 v34, vcc, s0, v58
	s_mov_b32 s0, 0xee000
	s_nop 0
	v_addc_co_u32_e32 v35, vcc, 0, v59, vcc
	v_add_co_u32_e32 v36, vcc, s0, v58
	s_mov_b32 s0, 0x118000
	s_nop 0
	v_addc_co_u32_e32 v37, vcc, 0, v59, vcc
	v_add_co_u32_e32 v42, vcc, s0, v58
	s_mov_b32 s0, 0x126000
	s_nop 0
	v_addc_co_u32_e32 v43, vcc, 0, v59, vcc
	v_add_co_u32_e32 v44, vcc, s0, v58
	s_mov_b32 s0, 0x150000
	s_nop 0
	v_addc_co_u32_e32 v45, vcc, 0, v59, vcc
	v_add_co_u32_e32 v50, vcc, s0, v58
	s_mov_b32 s0, 0x15e000
	s_nop 0
	v_addc_co_u32_e32 v51, vcc, 0, v59, vcc
	v_add_co_u32_e32 v52, vcc, s0, v58
	global_load_dwordx4 v[6:9], v[58:59], off nt
	s_nop 0
	global_load_dwordx4 v[2:5], v[2:3], off nt
	v_addc_co_u32_e32 v53, vcc, 0, v59, vcc
	v_add_co_u32_e32 v60, vcc, 0x188000, v58
	global_load_dwordx4 v[14:17], v[10:11], off nt
	s_nop 0
	global_load_dwordx4 v[10:13], v[12:13], off nt
	v_addc_co_u32_e32 v61, vcc, 0, v59, vcc
	v_add_co_u32_e32 v58, vcc, 0x196000, v58
	global_load_dwordx4 v[22:25], v[18:19], off nt
	s_nop 0
	global_load_dwordx4 v[18:21], v[20:21], off nt
	v_addc_co_u32_e32 v59, vcc, 0, v59, vcc
	global_load_dwordx4 v[30:33], v[26:27], off nt
	s_nop 0
	global_load_dwordx4 v[26:29], v[28:29], off nt
	s_nop 0
	global_load_dwordx4 v[38:41], v[34:35], off nt
	s_nop 0
	global_load_dwordx4 v[34:37], v[36:37], off nt
	s_nop 0
	global_load_dwordx4 v[46:49], v[42:43], off nt
	s_nop 0
	global_load_dwordx4 v[42:45], v[44:45], off nt
	s_nop 0
	global_load_dwordx4 v[54:57], v[50:51], off nt
	s_nop 0
	global_load_dwordx4 v[50:53], v[52:53], off nt
	s_nop 0
	global_load_dwordx4 v[62:65], v[60:61], off nt
	s_nop 0
	global_load_dwordx4 v[58:61], v[58:59], off nt
	s_cmp_eq_u64 s[40:41], 0
	s_cbranch_scc1 .LBB0_34
	s_ashr_i32 s15, s14, 31
	s_lshl_b64 s[0:1], s[14:15], 2
	s_add_u32 s0, s40, s0
	s_addc_u32 s1, s41, s1
	v_lshlrev_b32_e32 v66, 2, v66
	global_load_dwordx2 v[130:131], v66, s[0:1]
	global_load_dwordx2 v[132:133], v66, s[0:1] offset:16
	global_load_dwordx2 v[134:135], v66, s[0:1] offset:32
	global_load_dwordx2 v[136:137], v66, s[0:1] offset:48
	global_load_dwordx2 v[138:139], v66, s[0:1] offset:64
	global_load_dwordx2 v[140:141], v66, s[0:1] offset:80
	global_load_dwordx2 v[142:143], v66, s[0:1] offset:96
	global_load_dwordx2 v[144:145], v66, s[0:1] offset:112
	s_and_b64 vcc, exec, s[6:7]
	s_cbranch_vccnz .LBB0_167
	s_branch .LBB0_35

; #define GAS __attribute__((address_space(1)))
; template <bool UNCOND> DI void witem_load(const WItem& d, WRegs& R, int lane) {
;     const int n4 = lane & 31, kh = lane >> 5;
;     const float* src = d.W + (size_t)(d.k0 + 2 * kh) * d.N + d.src_col0 + 4 * n4;
; #pragma unroll
;     for (int i = 0; i < 8; ++i) { R.a[i] = *(const GAS f32x4*)(src + (size_t)(4 * i) * d.N); R.b[i] = *(const GAS f32x4*)(src + (size_t)(4 * i + 1) * d.N); }
;     if (UNCOND) {
;         const float* gp = d.gain ? d.gain + d.k0 + 2 * kh : src;
; #pragma unroll
;         for (int i = 0; i < 8; ++i) R.gg[i] = *(const GAS f32x2g*)(gp + 4 * i);
;         if (!d.gain) {
; #pragma unroll
;             for (int i = 0; i < 8; ++i) R.gg[i] = (f32x2g){1.f, 1.f}; }
;     } else if (d.gain) {
; #pragma unroll
;         for (int i = 0; i < 8; ++i) R.gg[i] = *(const GAS f32x2g*)(d.gain + d.k0 + 4 * i + 2 * kh); }
;     ...
;         const bool v1 = it + ST < wend && witem_decode<EARLY>(P, it + ST, d1);
;         if (PIPE) { if (!v1) d1 = d0; witem_load<true>(d1, R1, lane); } else if (v1) witem_load<false>(d1, R1, lane);
.LBB0_56:
	v_cndmask_b32_e64 v150, 0, 1, s[0:1]
	v_cmp_ne_u32_e64 s[6:7], 1, v150
	s_andn2_b64 vcc, exec, s[0:1]
	s_cbranch_vccnz .LBB0_60
	v_add_u32_e32 v68, s22, v146
	s_waitcnt lgkmcnt(0)
	v_mov_b64_e32 v[66:67], s[42:43]
	v_mad_i64_i32 v[66:67], s[0:1], v68, s27, v[66:67]
	s_ashr_i32 s21, s20, 31
	v_lshl_add_u64 v[66:67], s[20:21], 2, v[66:67]
	v_lshlrev_b32_e32 v150, 2, v148
	v_lshl_add_u64 v[110:111], v[66:67], 0, v[150:151]
	v_add_co_u32_e32 v70, vcc, 0xe000, v110
	s_cmp_eq_u64 s[40:41], 0
	s_nop 0
	v_addc_co_u32_e32 v71, vcc, 0, v111, vcc
	v_add_co_u32_e32 v74, vcc, 0x38000, v110
	global_load_dwordx4 v[66:69], v[110:111], off nt
	s_nop 0
	global_load_dwordx4 v[70:73], v[70:71], off nt
	v_addc_co_u32_e32 v75, vcc, 0, v111, vcc
	v_add_co_u32_e32 v78, vcc, 0x46000, v110
	s_nop 1
	v_addc_co_u32_e32 v79, vcc, 0, v111, vcc
	v_add_co_u32_e32 v82, vcc, 0x70000, v110
	global_load_dwordx4 v[74:77], v[74:75], off nt
	s_nop 0
	global_load_dwordx4 v[78:81], v[78:79], off nt
	v_addc_co_u32_e32 v83, vcc, 0, v111, vcc
	v_add_co_u32_e32 v86, vcc, 0x7e000, v110
	s_nop 1
	v_addc_co_u32_e32 v87, vcc, 0, v111, vcc
	v_add_co_u32_e32 v90, vcc, 0xa8000, v110
	global_load_dwordx4 v[82:85], v[82:83], off nt
	s_nop 0
	global_load_dwordx4 v[86:89], v[86:87], off nt
	v_addc_co_u32_e32 v91, vcc, 0, v111, vcc
	v_add_co_u32_e32 v94, vcc, 0xb6000, v110
	s_nop 1
	v_addc_co_u32_e32 v95, vcc, 0, v111, vcc
	v_add_co_u32_e32 v98, vcc, 0xe0000, v110
	global_load_dwordx4 v[90:93], v[90:91], off nt
	s_nop 0
	global_load_dwordx4 v[94:97], v[94:95], off nt
	v_addc_co_u32_e32 v99, vcc, 0, v111, vcc
	v_add_co_u32_e32 v102, vcc, 0xee000, v110
	s_nop 1
	v_addc_co_u32_e32 v103, vcc, 0, v111, vcc
	global_load_dwordx4 v[98:101], v[98:99], off nt
	s_nop 0
	global_load_dwordx4 v[114:117], v[102:103], off nt
	v_add_co_u32_e32 v102, vcc, 0x118000, v110
	s_nop 1
	v_addc_co_u32_e32 v103, vcc, 0, v111, vcc
	v_add_co_u32_e32 v106, vcc, 0x126000, v110
	s_nop 1
	v_addc_co_u32_e32 v107, vcc, 0, v111, vcc
	global_load_dwordx4 v[102:105], v[102:103], off nt
	s_nop 0
	global_load_dwordx4 v[118:121], v[106:107], off nt
	v_add_co_u32_e32 v106, vcc, 0x150000, v110
	s_nop 1
	v_addc_co_u32_e32 v107, vcc, 0, v111, vcc
	v_add_co_u32_e32 v112, vcc, 0x15e000, v110
	s_nop 1
	v_addc_co_u32_e32 v113, vcc, 0, v111, vcc
	global_load_dwordx4 v[106:109], v[106:107], off nt
	s_nop 0
	global_load_dwordx4 v[122:125], v[112:113], off nt
	v_add_co_u32_e32 v112, vcc, 0x188000, v110
	s_nop 1
	v_addc_co_u32_e32 v113, vcc, 0, v111, vcc
	v_add_co_u32_e32 v126, vcc, 0x196000, v110
	s_nop 1
	v_addc_co_u32_e32 v127, vcc, 0, v111, vcc
	global_load_dwordx4 v[110:113], v[112:113], off nt
	s_nop 0
	global_load_dwordx4 v[126:129], v[126:127], off nt
	s_cbranch_scc1 .LBB0_59
	s_ashr_i32 s23, s22, 31
	s_lshl_b64 s[0:1], s[22:23], 2
	s_add_u32 s0, s40, s0
	s_addc_u32 s1, s41, s1
	v_lshlrev_b32_e32 v150, 2, v146
	global_load_dwordx2 v[152:153], v150, s[0:1]
	global_load_dwordx2 v[154:155], v150, s[0:1] offset:16
	global_load_dwordx2 v[156:157], v150, s[0:1] offset:32
	global_load_dwordx2 v[158:159], v150, s[0:1] offset:48
	global_load_dwordx2 v[160:161], v150, s[0:1] offset:64
	global_load_dwordx2 v[162:163], v150, s[0:1] offset:80
	global_load_dwordx2 v[164:165], v150, s[0:1] offset:96
	global_load_dwordx2 v[166:167], v150, s[0:1] offset:112
	s_branch .LBB0_60

; #define GAS __attribute__((address_space(1)))
; template <bool UNCOND> DI void witem_load(const WItem& d, WRegs& R, int lane) {
;     const int n4 = lane & 31, kh = lane >> 5;
;     const float* src = d.W + (size_t)(d.k0 + 2 * kh) * d.N + d.src_col0 + 4 * n4;
; #pragma unroll
;     for (int i = 0; i < 8; ++i) { R.a[i] = *(const GAS f32x4*)(src + (size_t)(4 * i) * d.N); R.b[i] = *(const GAS f32x4*)(src + (size_t)(4 * i + 1) * d.N); }
;     if (UNCOND) {
;         const float* gp = d.gain ? d.gain + d.k0 + 2 * kh : src;
; #pragma unroll
;         for (int i = 0; i < 8; ++i) R.gg[i] = *(const GAS f32x2g*)(gp + 4 * i);
;         if (!d.gain) {
; #pragma unroll
;             for (int i = 0; i < 8; ++i) R.gg[i] = (f32x2g){1.f, 1.f}; }
;     } else if (d.gain) {
; #pragma unroll
;         for (int i = 0; i < 8; ++i) R.gg[i] = *(const GAS f32x2g*)(d.gain + d.k0 + 4 * i + 2 * kh); }
;     ...
;         v0 = it + 2 * ST < wend && witem_decode<EARLY>(P, it + 2 * ST, d0);
;         if (PIPE) { if (!v0) d0 = d1; witem_load<true>(d0, R0, lane); } else if (v0) witem_load<false>(d0, R0, lane);
.LBB0_121:
	s_andn2_b64 vcc, exec, s[0:1]
	s_cbranch_vccnz .LBB0_125
	v_add_u32_e32 v4, s14, v146
	v_mov_b64_e32 v[2:3], s[42:43]
	v_mad_i64_i32 v[2:3], s[0:1], v4, s27, v[2:3]
	s_ashr_i32 s13, s12, 31
	v_lshl_add_u64 v[2:3], s[12:13], 2, v[2:3]
	v_lshlrev_b32_e32 v150, 2, v148
	v_lshl_add_u64 v[58:59], v[2:3], 0, v[150:151]
	v_add_co_u32_e32 v2, vcc, 0xe000, v58
	s_cmp_eq_u64 s[40:41], 0
	s_nop 0
	v_addc_co_u32_e32 v3, vcc, 0, v59, vcc
	v_add_co_u32_e32 v10, vcc, 0x38000, v58
	global_load_dwordx4 v[6:9], v[58:59], off nt
	s_nop 0
	global_load_dwordx4 v[2:5], v[2:3], off nt
	v_addc_co_u32_e32 v11, vcc, 0, v59, vcc
	v_add_co_u32_e32 v12, vcc, 0x46000, v58
	s_nop 1
	v_addc_co_u32_e32 v13, vcc, 0, v59, vcc
	v_add_co_u32_e32 v18, vcc, 0x70000, v58
	global_load_dwordx4 v[14:17], v[10:11], off nt
	s_nop 0
	global_load_dwordx4 v[10:13], v[12:13], off nt
	v_addc_co_u32_e32 v19, vcc, 0, v59, vcc
	v_add_co_u32_e32 v20, vcc, 0x7e000, v58
	s_nop 1
	v_addc_co_u32_e32 v21, vcc, 0, v59, vcc
	v_add_co_u32_e32 v26, vcc, 0xa8000, v58
	global_load_dwordx4 v[22:25], v[18:19], off nt
	s_nop 0
	global_load_dwordx4 v[18:21], v[20:21], off nt
	v_addc_co_u32_e32 v27, vcc, 0, v59, vcc
	v_add_co_u32_e32 v28, vcc, 0xb6000, v58
	s_nop 1
	v_addc_co_u32_e32 v29, vcc, 0, v59, vcc
	v_add_co_u32_e32 v34, vcc, 0xe0000, v58
	global_load_dwordx4 v[30:33], v[26:27], off nt
	s_nop 0
	global_load_dwordx4 v[26:29], v[28:29], off nt
	v_addc_co_u32_e32 v35, vcc, 0, v59, vcc
	v_add_co_u32_e32 v36, vcc, 0xee000, v58
	s_nop 1
	v_addc_co_u32_e32 v37, vcc, 0, v59, vcc
	v_add_co_u32_e32 v42, vcc, 0x118000, v58
	global_load_dwordx4 v[38:41], v[34:35], off nt
	s_nop 0
	global_load_dwordx4 v[34:37], v[36:37], off nt
	v_addc_co_u32_e32 v43, vcc, 0, v59, vcc
	v_add_co_u32_e32 v44, vcc, 0x126000, v58
	s_nop 1
	v_addc_co_u32_e32 v45, vcc, 0, v59, vcc
	v_add_co_u32_e32 v50, vcc, 0x150000, v58
	global_load_dwordx4 v[46:49], v[42:43], off nt
	s_nop 0
	global_load_dwordx4 v[42:45], v[44:45], off nt
	v_addc_co_u32_e32 v51, vcc, 0, v59, vcc
	v_add_co_u32_e32 v52, vcc, 0x15e000, v58
	s_nop 1
	v_addc_co_u32_e32 v53, vcc, 0, v59, vcc
	v_add_co_u32_e32 v60, vcc, 0x188000, v58
	global_load_dwordx4 v[54:57], v[50:51], off nt
	s_nop 0
	global_load_dwordx4 v[50:53], v[52:53], off nt
	v_addc_co_u32_e32 v61, vcc, 0, v59, vcc
	v_add_co_u32_e32 v58, vcc, 0x196000, v58
	s_nop 1
	v_addc_co_u32_e32 v59, vcc, 0, v59, vcc
	global_load_dwordx4 v[62:65], v[60:61], off nt
	s_nop 0
	global_load_dwordx4 v[58:61], v[58:59], off nt
	s_cbranch_scc1 .LBB0_124
	s_ashr_i32 s15, s14, 31
	s_lshl_b64 s[0:1], s[14:15], 2
	s_add_u32 s0, s40, s0
	s_addc_u32 s1, s41, s1
	v_lshlrev_b32_e32 v144, 2, v146
	global_load_dwordx2 v[130:131], v144, s[0:1]
	global_load_dwordx2 v[132:133], v144, s[0:1] offset:16
	global_load_dwordx2 v[134:135], v144, s[0:1] offset:32
	global_load_dwordx2 v[136:137], v144, s[0:1] offset:48
	global_load_dwordx2 v[138:139], v144, s[0:1] offset:64
	global_load_dwordx2 v[140:141], v144, s[0:1] offset:80
	global_load_dwordx2 v[142:143], v144, s[0:1] offset:96
	s_nop 0
	global_load_dwordx2 v[144:145], v144, s[0:1] offset:112
	s_branch .LBB0_125

; __device__ __forceinline__ unsigned pk_bf16(float lo, float hi) { const f32x2 f = {lo, hi}; const bf16v2 r = __builtin_convertvector(f, bf16v2); return __builtin_bit_cast(unsigned, r); }
; #define GAS __attribute__((address_space(1)))
; DI void row_to_bf16(const float* __restrict__ xrow, bf16* __restrict__ obase, int m, float* __restrict__ ssq, int lane) {
;     const GAS f32x4* xr = (const GAS f32x4*)xrow + lane; float s = 0.f; f32x4 v[16];
; #pragma unroll
;     for (int j = 0; j < 16; ++j) v[j] = xr[64 * j];
;     asm volatile("" ::: "memory");
; #pragma unroll
;     for (int j = 0; j < 16; ++j) { s += (v[j].x * v[j].x + v[j].y * v[j].y) + (v[j].z * v[j].z + v[j].w * v[j].w); v2u w; w.x = pk_bf16(v[j].x, v[j].y); w.y = pk_bf16(v[j].z, v[j].w);
;         *(GAS v2u*)(obase + pg8::blk_elem(m, 4 * lane + 256 * j, DM)) = w; }
;     s = wave_sum(s); if (lane == 0) *ssq = s;
; }
; DI void p0_prologue(const Ptrs& P, LAS unsigned char* lds, int gw, int NGW, int wave, int lane) {
;     ...
;     for (int m = gw; m < M; m += NGW) row_to_bf16(P.x + (size_t)m * DM, (bf16*)(ws + WS_HB), m, (float*)(ws + WS_SSQ0) + m, lane);
.LBB0_170:
	global_load_dwordx4 v[42:45], v[28:29], off nt
	global_load_dwordx4 v[46:49], v[28:29], off offset:1024 nt
	global_load_dwordx4 v[50:53], v[28:29], off offset:2048 nt
	global_load_dwordx4 v[54:57], v[28:29], off offset:3072 nt
	v_add_co_u32_e32 v2, vcc, 0x1000, v28
	s_lshr_b32 s16, s9, 3
	s_waitcnt lgkmcnt(0)
	v_addc_co_u32_e32 v3, vcc, 0, v29, vcc
	global_load_dwordx4 v[58:61], v[2:3], off nt
	global_load_dwordx4 v[62:65], v[2:3], off offset:1024 nt
	global_load_dwordx4 v[66:69], v[2:3], off offset:2048 nt
	global_load_dwordx4 v[70:73], v[2:3], off offset:3072 nt
	v_add_co_u32_e32 v4, vcc, 0x2000, v28
	s_lshr_b32 s18, s3, 4
	s_nop 0
	v_addc_co_u32_e32 v5, vcc, 0, v29, vcc
	global_load_dwordx4 v[74:77], v[4:5], off nt
	global_load_dwordx4 v[78:81], v[4:5], off offset:1024 nt
	global_load_dwordx4 v[18:21], v[4:5], off offset:2048 nt
	global_load_dwordx4 v[14:17], v[4:5], off offset:3072 nt
	v_and_or_b32 v6, s16, 14, v32
	s_and_b32 s16, s18, 32
	v_add_co_u32_e32 v2, vcc, 0x3000, v28
	s_and_b32 s17, s3, 0x3c0
	v_lshlrev_b32_e32 v83, 10, v6
	v_mov_b32_e32 v6, s16
	v_addc_co_u32_e32 v3, vcc, 0, v29, vcc
	v_bitop3_b32 v85, s17, v6, v34 bitop3:0x36
	global_load_dwordx4 v[22:25], v[2:3], off nt
	global_load_dwordx4 v[10:13], v[2:3], off offset:1024 nt
	global_load_dwordx4 v[6:9], v[2:3], off offset:2048 nt
	s_nop 0
	global_load_dwordx4 v[2:5], v[2:3], off offset:3072 nt
	s_ashr_i32 s12, s9, 2
	s_andn2_b32 s12, s12, 63
	v_or_b32_e32 v30, s12, v33
	v_ashrrev_i32_e32 v31, 31, v30
	v_lshlrev_b64 v[86:87], 15, v[30:31]
	s_and_b32 s13, s14, 0x4000
	v_or_b32_e32 v82, 4, v30
	v_or_b32_e32 v84, 8, v30
	v_or3_b32 v94, v85, v83, s13
	v_ashrrev_i32_e32 v83, 31, v82
	v_ashrrev_i32_e32 v85, 31, v84
	v_lshlrev_b64 v[82:83], 15, v[82:83]
	v_lshlrev_b64 v[84:85], 15, v[84:85]
	v_bitop3_b32 v86, v86, -2, v94 bitop3:0xc8
	v_bitop3_b32 v82, v82, -2, v94 bitop3:0xc8
	v_bitop3_b32 v84, v84, -2, v94 bitop3:0xc8
	v_lshl_add_u64 v[86:87], s[82:83], 0, v[86:87]
	v_lshl_add_u64 v[82:83], s[82:83], 0, v[82:83]
	v_lshl_add_u64 v[84:85], s[82:83], 0, v[84:85]
	v_cmp_lt_i32_e32 vcc, v36, v35
	s_waitcnt vmcnt(15)
	v_mul_f32_e32 v31, v43, v43
	v_mul_f32_e32 v95, v45, v45
	v_cvt_pk_bf16_f32 v88, v42, v43
	v_cvt_pk_bf16_f32 v89, v44, v45
	s_waitcnt vmcnt(14)
	v_mul_f32_e32 v43, v47, v47
	v_mul_f32_e32 v45, v49, v49
	v_cvt_pk_bf16_f32 v90, v46, v47
	v_cvt_pk_bf16_f32 v91, v48, v49
	s_waitcnt vmcnt(13)
	v_mul_f32_e32 v47, v51, v51
	v_mul_f32_e32 v49, v53, v53
	v_fmac_f32_e32 v31, v42, v42
	v_fmac_f32_e32 v95, v44, v44
	v_fmac_f32_e32 v43, v46, v46
	v_fmac_f32_e32 v45, v48, v48
	v_fmac_f32_e32 v47, v50, v50
	v_fmac_f32_e32 v49, v52, v52
	v_add_f32_e32 v31, v31, v95
	v_add_f32_e32 v42, v43, v45
	v_add_f32_e32 v43, v47, v49
	v_add_f32_e32 v31, v31, v42
	v_or_b32_e32 v44, 12, v30
	v_add_f32_e32 v31, v31, v43
	s_waitcnt vmcnt(12)
	v_mul_f32_e32 v42, v55, v55
	v_mul_f32_e32 v43, v57, v57
	v_ashrrev_i32_e32 v45, 31, v44
	v_fmac_f32_e32 v42, v54, v54
	v_fmac_f32_e32 v43, v56, v56
	v_lshlrev_b64 v[44:45], 15, v[44:45]
	v_add_f32_e32 v42, v42, v43
	v_bitop3_b32 v44, v44, -2, v94 bitop3:0xc8
	v_cvt_pk_bf16_f32 v92, v50, v51
	v_cvt_pk_bf16_f32 v93, v52, v53
	v_add_f32_e32 v31, v31, v42
	v_cvt_pk_bf16_f32 v42, v54, v55
	v_cvt_pk_bf16_f32 v43, v56, v57
	v_lshl_add_u64 v[44:45], s[82:83], 0, v[44:45]
	global_store_dwordx2 v[86:87], v[88:89], off
	global_store_dwordx2 v[82:83], v[90:91], off
	global_store_dwordx2 v[84:85], v[92:93], off
	global_store_dwordx2 v[44:45], v[42:43], off
	v_or_b32_e32 v44, 16, v30
	s_waitcnt vmcnt(15)
	v_mul_f32_e32 v42, v59, v59
	v_mul_f32_e32 v43, v61, v61
	v_ashrrev_i32_e32 v45, 31, v44
	v_fmac_f32_e32 v42, v58, v58
	v_fmac_f32_e32 v43, v60, v60
	v_lshlrev_b64 v[44:45], 15, v[44:45]
	v_add_f32_e32 v42, v42, v43
	v_bitop3_b32 v44, v44, -2, v94 bitop3:0xc8
	v_add_f32_e32 v31, v31, v42
	v_cvt_pk_bf16_f32 v42, v58, v59
	v_cvt_pk_bf16_f32 v43, v60, v61
	v_lshl_add_u64 v[44:45], s[82:83], 0, v[44:45]
	global_store_dwordx2 v[44:45], v[42:43], off
	v_or_b32_e32 v44, 20, v30
	s_waitcnt vmcnt(15)
	v_mul_f32_e32 v42, v63, v63
	v_mul_f32_e32 v43, v65, v65
	v_ashrrev_i32_e32 v45, 31, v44
	v_fmac_f32_e32 v42, v62, v62
	v_fmac_f32_e32 v43, v64, v64
	v_lshlrev_b64 v[44:45], 15, v[44:45]
	v_add_f32_e32 v42, v42, v43
	v_bitop3_b32 v44, v44, -2, v94 bitop3:0xc8
	v_add_f32_e32 v31, v31, v42
	v_cvt_pk_bf16_f32 v42, v62, v63
	v_cvt_pk_bf16_f32 v43, v64, v65
	v_lshl_add_u64 v[44:45], s[82:83], 0, v[44:45]
	global_store_dwordx2 v[44:45], v[42:43], off
	v_or_b32_e32 v44, 24, v30
	s_waitcnt vmcnt(15)
	v_mul_f32_e32 v42, v67, v67
	v_mul_f32_e32 v43, v69, v69
	v_ashrrev_i32_e32 v45, 31, v44
	v_fmac_f32_e32 v42, v66, v66
	v_fmac_f32_e32 v43, v68, v68
	v_lshlrev_b64 v[44:45], 15, v[44:45]
	v_add_f32_e32 v42, v42, v43
	v_bitop3_b32 v44, v44, -2, v94 bitop3:0xc8
	v_add_f32_e32 v31, v31, v42
	v_cvt_pk_bf16_f32 v42, v66, v67
	v_cvt_pk_bf16_f32 v43, v68, v69
	v_lshl_add_u64 v[44:45], s[82:83], 0, v[44:45]
	global_store_dwordx2 v[44:45], v[42:43], off
	v_or_b32_e32 v44, 28, v30
	s_waitcnt vmcnt(15)
; __device__ __forceinline__ unsigned pk_bf16(float lo, float hi) { const f32x2 f = {lo, hi}; const bf16v2 r = __builtin_convertvector(f, bf16v2); return __builtin_bit_cast(unsigned, r); }
; #define GAS __attribute__((address_space(1)))
; DI void row_to_bf16(const float* __restrict__ xrow, bf16* __restrict__ obase, int m, float* __restrict__ ssq, int lane) {
;     ...
;     for (int j = 0; j < 16; ++j) { s += (v[j].x * v[j].x + v[j].y * v[j].y) + (v[j].z * v[j].z + v[j].w * v[j].w); v2u w; w.x = pk_bf16(v[j].x, v[j].y); w.y = pk_bf16(v[j].z, v[j].w);
;         *(GAS v2u*)(obase + pg8::blk_elem(m, 4 * lane + 256 * j, DM)) = w; }
;     s = wave_sum(s); if (lane == 0) *ssq = s;
	v_mul_f32_e32 v42, v71, v71
	v_mul_f32_e32 v43, v73, v73
	v_ashrrev_i32_e32 v45, 31, v44
	v_fmac_f32_e32 v42, v70, v70
	v_fmac_f32_e32 v43, v72, v72
	v_lshlrev_b64 v[44:45], 15, v[44:45]
	v_add_f32_e32 v42, v42, v43
	v_bitop3_b32 v44, v44, -2, v94 bitop3:0xc8
	v_add_f32_e32 v31, v31, v42
	v_cvt_pk_bf16_f32 v42, v70, v71
	v_cvt_pk_bf16_f32 v43, v72, v73
	v_lshl_add_u64 v[44:45], s[82:83], 0, v[44:45]
	global_store_dwordx2 v[44:45], v[42:43], off
	v_or_b32_e32 v44, 32, v30
	s_waitcnt vmcnt(15)
	v_mul_f32_e32 v42, v75, v75
	v_mul_f32_e32 v43, v77, v77
	v_ashrrev_i32_e32 v45, 31, v44
	v_fmac_f32_e32 v42, v74, v74
	v_fmac_f32_e32 v43, v76, v76
	v_lshlrev_b64 v[44:45], 15, v[44:45]
	v_add_f32_e32 v42, v42, v43
	v_bitop3_b32 v44, v44, -2, v94 bitop3:0xc8
	v_add_f32_e32 v31, v31, v42
	v_cvt_pk_bf16_f32 v42, v74, v75
	v_cvt_pk_bf16_f32 v43, v76, v77
	v_lshl_add_u64 v[44:45], s[82:83], 0, v[44:45]
	global_store_dwordx2 v[44:45], v[42:43], off
	v_or_b32_e32 v44, 36, v30
	s_waitcnt vmcnt(15)
	v_mul_f32_e32 v42, v79, v79
	v_mul_f32_e32 v43, v81, v81
	v_ashrrev_i32_e32 v45, 31, v44
	v_fmac_f32_e32 v42, v78, v78
	v_fmac_f32_e32 v43, v80, v80
	v_lshlrev_b64 v[44:45], 15, v[44:45]
	v_add_f32_e32 v42, v42, v43
	v_bitop3_b32 v44, v44, -2, v94 bitop3:0xc8
	v_add_f32_e32 v31, v31, v42
	v_cvt_pk_bf16_f32 v42, v78, v79
	v_cvt_pk_bf16_f32 v43, v80, v81
	v_lshl_add_u64 v[44:45], s[82:83], 0, v[44:45]
	global_store_dwordx2 v[44:45], v[42:43], off
	s_waitcnt vmcnt(15)
	v_mul_f32_e32 v42, v19, v19
	v_mul_f32_e32 v43, v21, v21
	v_fmac_f32_e32 v42, v18, v18
	v_fmac_f32_e32 v43, v20, v20
	v_cvt_pk_bf16_f32 v18, v18, v19
	v_cvt_pk_bf16_f32 v19, v20, v21
	v_or_b32_e32 v20, 40, v30
	v_ashrrev_i32_e32 v21, 31, v20
	v_lshlrev_b64 v[20:21], 15, v[20:21]
	v_bitop3_b32 v20, v20, -2, v94 bitop3:0xc8
	v_lshl_add_u64 v[20:21], s[82:83], 0, v[20:21]
	global_store_dwordx2 v[20:21], v[18:19], off
	s_waitcnt vmcnt(15)
	v_mul_f32_e32 v18, v15, v15
	v_mul_f32_e32 v19, v17, v17
	v_fmac_f32_e32 v18, v14, v14
	v_fmac_f32_e32 v19, v16, v16
	v_cvt_pk_bf16_f32 v14, v14, v15
	v_cvt_pk_bf16_f32 v15, v16, v17
	v_or_b32_e32 v16, 44, v30
	v_ashrrev_i32_e32 v17, 31, v16
	v_lshlrev_b64 v[16:17], 15, v[16:17]
	v_bitop3_b32 v16, v16, -2, v94 bitop3:0xc8
	v_lshl_add_u64 v[16:17], s[82:83], 0, v[16:17]
	global_store_dwordx2 v[16:17], v[14:15], off
	v_or_b32_e32 v16, 48, v30
	v_add_f32_e32 v42, v42, v43
	s_waitcnt vmcnt(15)
	v_mul_f32_e32 v14, v23, v23
	v_mul_f32_e32 v15, v25, v25
	v_ashrrev_i32_e32 v17, 31, v16
	v_add_f32_e32 v31, v31, v42
	v_add_f32_e32 v18, v18, v19
	v_fmac_f32_e32 v14, v22, v22
	v_fmac_f32_e32 v15, v24, v24
	v_lshlrev_b64 v[16:17], 15, v[16:17]
	v_add_f32_e32 v18, v31, v18
	v_add_f32_e32 v14, v14, v15
	v_bitop3_b32 v16, v16, -2, v94 bitop3:0xc8
	v_add_f32_e32 v18, v18, v14
	v_cvt_pk_bf16_f32 v14, v22, v23
	v_cvt_pk_bf16_f32 v15, v24, v25
	v_lshl_add_u64 v[16:17], s[82:83], 0, v[16:17]
	global_store_dwordx2 v[16:17], v[14:15], off
	s_waitcnt vmcnt(15)
	v_mul_f32_e32 v14, v11, v11
	v_mul_f32_e32 v15, v13, v13
	v_fmac_f32_e32 v14, v10, v10
	v_fmac_f32_e32 v15, v12, v12
	v_add_f32_e32 v14, v14, v15
	s_waitcnt vmcnt(14)
	v_mul_f32_e32 v15, v7, v7
	v_mul_f32_e32 v16, v9, v9
	v_fmac_f32_e32 v15, v6, v6
	v_fmac_f32_e32 v16, v8, v8
	v_add_f32_e32 v14, v18, v14
	v_add_f32_e32 v15, v15, v16
	v_add_f32_e32 v14, v14, v15
	s_waitcnt vmcnt(13)
	v_mul_f32_e32 v15, v3, v3
	v_mul_f32_e32 v16, v5, v5
	v_fmac_f32_e32 v15, v2, v2
	v_fmac_f32_e32 v16, v4, v4
	v_add_f32_e32 v15, v15, v16
	v_add_f32_e32 v14, v14, v15
	v_cndmask_b32_e32 v15, v26, v36, vcc
	v_lshlrev_b32_e32 v15, 2, v15
	ds_bpermute_b32 v15, v15, v14
	v_cmp_lt_i32_e32 vcc, v37, v35
	v_cvt_pk_bf16_f32 v10, v10, v11
	v_cvt_pk_bf16_f32 v11, v12, v13
	v_or_b32_e32 v12, 52, v30
	s_waitcnt lgkmcnt(0)
	v_add_f32_e32 v14, v14, v15
	v_cndmask_b32_e32 v15, v26, v37, vcc
	v_lshlrev_b32_e32 v15, 2, v15
	v_ashrrev_i32_e32 v13, 31, v12
	ds_bpermute_b32 v15, v15, v14
	v_lshlrev_b64 v[12:13], 15, v[12:13]
	v_bitop3_b32 v12, v12, -2, v94 bitop3:0xc8
	v_lshl_add_u64 v[12:13], s[82:83], 0, v[12:13]
	v_cmp_lt_i32_e32 vcc, v38, v35
	global_store_dwordx2 v[12:13], v[10:11], off
	s_waitcnt lgkmcnt(0)
	v_add_f32_e32 v10, v14, v15
	v_cndmask_b32_e32 v11, v26, v38, vcc
	v_lshlrev_b32_e32 v11, 2, v11
	ds_bpermute_b32 v11, v11, v10
	v_cmp_lt_i32_e32 vcc, v39, v35
	v_cvt_pk_bf16_f32 v6, v6, v7
	v_cvt_pk_bf16_f32 v7, v8, v9
	v_or_b32_e32 v8, 56, v30
	s_waitcnt lgkmcnt(0)
	v_add_f32_e32 v10, v10, v11
	v_cndmask_b32_e32 v11, v26, v39, vcc
	v_lshlrev_b32_e32 v11, 2, v11
	v_ashrrev_i32_e32 v9, 31, v8
	ds_bpermute_b32 v11, v11, v10
	v_lshlrev_b64 v[8:9], 15, v[8:9]
	v_bitop3_b32 v8, v8, -2, v94 bitop3:0xc8
	v_lshl_add_u64 v[8:9], s[82:83], 0, v[8:9]
	v_cmp_lt_i32_e32 vcc, v40, v35
	global_store_dwordx2 v[8:9], v[6:7], off
	s_waitcnt lgkmcnt(0)
	v_add_f32_e32 v8, v10, v11
	v_cndmask_b32_e32 v6, v26, v40, vcc
	v_lshlrev_b32_e32 v6, 2, v6
	ds_bpermute_b32 v9, v6, v8
	v_cmp_lt_i32_e32 vcc, v41, v35
	v_cvt_pk_bf16_f32 v6, v2, v3
	v_cvt_pk_bf16_f32 v7, v4, v5
	v_cndmask_b32_e32 v3, v26, v41, vcc
	s_waitcnt lgkmcnt(0)
	v_add_f32_e32 v2, v8, v9
	v_lshlrev_b32_e32 v3, 2, v3
	v_or_b32_e32 v4, 60, v30
	ds_bpermute_b32 v3, v3, v2
	v_ashrrev_i32_e32 v5, 31, v4
	v_lshlrev_b64 v[4:5], 15, v[4:5]
	v_bitop3_b32 v4, v4, -2, v94 bitop3:0xc8
	v_lshl_add_u64 v[4:5], s[82:83], 0, v[4:5]
	global_store_dwordx2 v[4:5], v[6:7], off
	s_and_saveexec_b64 s[12:13], s[6:7]
	s_cbranch_execz .LBB0_169
	s_waitcnt lgkmcnt(0)
	v_add_f32_e32 v2, v2, v3
	global_store_dword v27, v2, s[0:1]
	s_branch .LBB0_169

; __device__ __forceinline__ unsigned pk_bf16(float lo, float hi) { const f32x2 f = {lo, hi}; const bf16v2 r = __builtin_convertvector(f, bf16v2); return __builtin_bit_cast(unsigned, r); }
; #define GAS __attribute__((address_space(1)))
; DI void row_to_bf16(const float* __restrict__ xrow, bf16* __restrict__ obase, int m, float* __restrict__ ssq, int lane) {
;     const GAS f32x4* xr = (const GAS f32x4*)xrow + lane; float s = 0.f; f32x4 v[16];
; #pragma unroll
;     for (int j = 0; j < 16; ++j) v[j] = xr[64 * j];
;     asm volatile("" ::: "memory");
; #pragma unroll
;     for (int j = 0; j < 16; ++j) { s += (v[j].x * v[j].x + v[j].y * v[j].y) + (v[j].z * v[j].z + v[j].w * v[j].w); v2u w; w.x = pk_bf16(v[j].x, v[j].y); w.y = pk_bf16(v[j].z, v[j].w);
;         *(GAS v2u*)(obase + pg8::blk_elem(m, 4 * lane + 256 * j, DM)) = w; }
;     s = wave_sum(s); if (lane == 0) *ssq = s;
; }
; DI void p0_prologue(const Ptrs& P, LAS unsigned char* lds, int gw, int NGW, int wave, int lane) {
;     ...
;     for (int m = gw; m < BATCH * NMEM; m += NGW) row_to_bf16(P.mem + (size_t)m * DM, (bf16*)(ws + WS_MB), m, (float*)(ws + WS_SSQM) + m, lane);
.LBB0_175:
	global_load_dwordx4 v[42:45], v[28:29], off nt
	global_load_dwordx4 v[46:49], v[28:29], off offset:1024 nt
	global_load_dwordx4 v[50:53], v[28:29], off offset:2048 nt
	global_load_dwordx4 v[54:57], v[28:29], off offset:3072 nt
	v_add_co_u32_e32 v2, vcc, 0x1000, v28
	s_lshr_b32 s18, s9, 3
	s_waitcnt lgkmcnt(0)
	v_addc_co_u32_e32 v3, vcc, 0, v29, vcc
	global_load_dwordx4 v[58:61], v[2:3], off nt
	global_load_dwordx4 v[62:65], v[2:3], off offset:1024 nt
	global_load_dwordx4 v[66:69], v[2:3], off offset:2048 nt
	global_load_dwordx4 v[70:73], v[2:3], off offset:3072 nt
	v_add_co_u32_e32 v4, vcc, 0x2000, v28
	s_lshr_b32 s20, s3, 4
	s_nop 0
	v_addc_co_u32_e32 v5, vcc, 0, v29, vcc
	global_load_dwordx4 v[74:77], v[4:5], off nt
	global_load_dwordx4 v[78:81], v[4:5], off offset:1024 nt
	global_load_dwordx4 v[18:21], v[4:5], off offset:2048 nt
	global_load_dwordx4 v[14:17], v[4:5], off offset:3072 nt
	v_and_or_b32 v6, s18, 14, v32
	s_and_b32 s18, s20, 32
	v_add_co_u32_e32 v2, vcc, 0x3000, v28
	s_and_b32 s19, s3, 0x3c0
	v_lshlrev_b32_e32 v83, 10, v6
	v_mov_b32_e32 v6, s18
	v_addc_co_u32_e32 v3, vcc, 0, v29, vcc
	v_bitop3_b32 v85, s19, v6, v34 bitop3:0x36
	global_load_dwordx4 v[22:25], v[2:3], off nt
	global_load_dwordx4 v[10:13], v[2:3], off offset:1024 nt
	global_load_dwordx4 v[6:9], v[2:3], off offset:2048 nt
	s_nop 0
	global_load_dwordx4 v[2:5], v[2:3], off offset:3072 nt
	s_ashr_i32 s14, s9, 2
	s_andn2_b32 s14, s14, 63
	v_or_b32_e32 v30, s14, v33
	v_ashrrev_i32_e32 v31, 31, v30
	v_lshlrev_b64 v[86:87], 15, v[30:31]
	s_and_b32 s15, s16, 0x4000
	v_or_b32_e32 v82, 4, v30
	v_or_b32_e32 v84, 8, v30
	v_or3_b32 v94, v85, v83, s15
	v_ashrrev_i32_e32 v83, 31, v82
	v_ashrrev_i32_e32 v85, 31, v84
	v_lshlrev_b64 v[82:83], 15, v[82:83]
	v_lshlrev_b64 v[84:85], 15, v[84:85]
	v_bitop3_b32 v86, v86, -2, v94 bitop3:0xc8
	v_bitop3_b32 v82, v82, -2, v94 bitop3:0xc8
	v_bitop3_b32 v84, v84, -2, v94 bitop3:0xc8
	v_lshl_add_u64 v[86:87], s[0:1], 0, v[86:87]
	v_lshl_add_u64 v[82:83], s[0:1], 0, v[82:83]
	v_lshl_add_u64 v[84:85], s[0:1], 0, v[84:85]
	v_cmp_lt_i32_e32 vcc, v36, v35
	s_waitcnt vmcnt(15)
	v_mul_f32_e32 v31, v43, v43
	v_mul_f32_e32 v95, v45, v45
	v_cvt_pk_bf16_f32 v88, v42, v43
	v_cvt_pk_bf16_f32 v89, v44, v45
	s_waitcnt vmcnt(14)
	v_mul_f32_e32 v43, v47, v47
	v_mul_f32_e32 v45, v49, v49
	v_cvt_pk_bf16_f32 v90, v46, v47
	v_cvt_pk_bf16_f32 v91, v48, v49
	s_waitcnt vmcnt(13)
	v_mul_f32_e32 v47, v51, v51
	v_mul_f32_e32 v49, v53, v53
	v_fmac_f32_e32 v31, v42, v42
	v_fmac_f32_e32 v95, v44, v44
	v_fmac_f32_e32 v43, v46, v46
	v_fmac_f32_e32 v45, v48, v48
	v_fmac_f32_e32 v47, v50, v50
	v_fmac_f32_e32 v49, v52, v52
	v_add_f32_e32 v31, v31, v95
	v_add_f32_e32 v42, v43, v45
	v_add_f32_e32 v43, v47, v49
	v_add_f32_e32 v31, v31, v42
	v_or_b32_e32 v44, 12, v30
	v_add_f32_e32 v31, v31, v43
	s_waitcnt vmcnt(12)
	v_mul_f32_e32 v42, v55, v55
	v_mul_f32_e32 v43, v57, v57
	v_ashrrev_i32_e32 v45, 31, v44
	v_fmac_f32_e32 v42, v54, v54
	v_fmac_f32_e32 v43, v56, v56
	v_lshlrev_b64 v[44:45], 15, v[44:45]
	v_add_f32_e32 v42, v42, v43
	v_bitop3_b32 v44, v44, -2, v94 bitop3:0xc8
	v_cvt_pk_bf16_f32 v92, v50, v51
	v_cvt_pk_bf16_f32 v93, v52, v53
	v_add_f32_e32 v31, v31, v42
	v_cvt_pk_bf16_f32 v42, v54, v55
	v_cvt_pk_bf16_f32 v43, v56, v57
	v_lshl_add_u64 v[44:45], s[0:1], 0, v[44:45]
	global_store_dwordx2 v[86:87], v[88:89], off
	global_store_dwordx2 v[82:83], v[90:91], off
	global_store_dwordx2 v[84:85], v[92:93], off
	global_store_dwordx2 v[44:45], v[42:43], off
	v_or_b32_e32 v44, 16, v30
	s_waitcnt vmcnt(15)
	v_mul_f32_e32 v42, v59, v59
	v_mul_f32_e32 v43, v61, v61
	v_ashrrev_i32_e32 v45, 31, v44
	v_fmac_f32_e32 v42, v58, v58
	v_fmac_f32_e32 v43, v60, v60
	v_lshlrev_b64 v[44:45], 15, v[44:45]
	v_add_f32_e32 v42, v42, v43
	v_bitop3_b32 v44, v44, -2, v94 bitop3:0xc8
	v_add_f32_e32 v31, v31, v42
	v_cvt_pk_bf16_f32 v42, v58, v59
	v_cvt_pk_bf16_f32 v43, v60, v61
	v_lshl_add_u64 v[44:45], s[0:1], 0, v[44:45]
	global_store_dwordx2 v[44:45], v[42:43], off
	v_or_b32_e32 v44, 20, v30
	s_waitcnt vmcnt(15)
	v_mul_f32_e32 v42, v63, v63
	v_mul_f32_e32 v43, v65, v65
	v_ashrrev_i32_e32 v45, 31, v44
	v_fmac_f32_e32 v42, v62, v62
	v_fmac_f32_e32 v43, v64, v64
	v_lshlrev_b64 v[44:45], 15, v[44:45]
	v_add_f32_e32 v42, v42, v43
	v_bitop3_b32 v44, v44, -2, v94 bitop3:0xc8
	v_add_f32_e32 v31, v31, v42
	v_cvt_pk_bf16_f32 v42, v62, v63
	v_cvt_pk_bf16_f32 v43, v64, v65
	v_lshl_add_u64 v[44:45], s[0:1], 0, v[44:45]
	global_store_dwordx2 v[44:45], v[42:43], off
	v_or_b32_e32 v44, 24, v30
	s_waitcnt vmcnt(15)
	v_mul_f32_e32 v42, v67, v67
	v_mul_f32_e32 v43, v69, v69
	v_ashrrev_i32_e32 v45, 31, v44
	v_fmac_f32_e32 v42, v66, v66
	v_fmac_f32_e32 v43, v68, v68
	v_lshlrev_b64 v[44:45], 15, v[44:45]
	v_add_f32_e32 v42, v42, v43
	v_bitop3_b32 v44, v44, -2, v94 bitop3:0xc8
	v_add_f32_e32 v31, v31, v42
	v_cvt_pk_bf16_f32 v42, v66, v67
	v_cvt_pk_bf16_f32 v43, v68, v69
	v_lshl_add_u64 v[44:45], s[0:1], 0, v[44:45]
	global_store_dwordx2 v[44:45], v[42:43], off
	v_or_b32_e32 v44, 28, v30
	s_waitcnt vmcnt(15)
; __device__ __forceinline__ unsigned pk_bf16(float lo, float hi) { const f32x2 f = {lo, hi}; const bf16v2 r = __builtin_convertvector(f, bf16v2); return __builtin_bit_cast(unsigned, r); }
; #define GAS __attribute__((address_space(1)))
; DI void row_to_bf16(const float* __restrict__ xrow, bf16* __restrict__ obase, int m, float* __restrict__ ssq, int lane) {
;     ...
;     for (int j = 0; j < 16; ++j) { s += (v[j].x * v[j].x + v[j].y * v[j].y) + (v[j].z * v[j].z + v[j].w * v[j].w); v2u w; w.x = pk_bf16(v[j].x, v[j].y); w.y = pk_bf16(v[j].z, v[j].w);
;         *(GAS v2u*)(obase + pg8::blk_elem(m, 4 * lane + 256 * j, DM)) = w; }
;     s = wave_sum(s); if (lane == 0) *ssq = s;
	v_mul_f32_e32 v42, v71, v71
	v_mul_f32_e32 v43, v73, v73
	v_ashrrev_i32_e32 v45, 31, v44
	v_fmac_f32_e32 v42, v70, v70
	v_fmac_f32_e32 v43, v72, v72
	v_lshlrev_b64 v[44:45], 15, v[44:45]
	v_add_f32_e32 v42, v42, v43
	v_bitop3_b32 v44, v44, -2, v94 bitop3:0xc8
	v_add_f32_e32 v31, v31, v42
	v_cvt_pk_bf16_f32 v42, v70, v71
	v_cvt_pk_bf16_f32 v43, v72, v73
	v_lshl_add_u64 v[44:45], s[0:1], 0, v[44:45]
	global_store_dwordx2 v[44:45], v[42:43], off
	v_or_b32_e32 v44, 32, v30
	s_waitcnt vmcnt(15)
	v_mul_f32_e32 v42, v75, v75
	v_mul_f32_e32 v43, v77, v77
	v_ashrrev_i32_e32 v45, 31, v44
	v_fmac_f32_e32 v42, v74, v74
	v_fmac_f32_e32 v43, v76, v76
	v_lshlrev_b64 v[44:45], 15, v[44:45]
	v_add_f32_e32 v42, v42, v43
	v_bitop3_b32 v44, v44, -2, v94 bitop3:0xc8
	v_add_f32_e32 v31, v31, v42
	v_cvt_pk_bf16_f32 v42, v74, v75
	v_cvt_pk_bf16_f32 v43, v76, v77
	v_lshl_add_u64 v[44:45], s[0:1], 0, v[44:45]
	global_store_dwordx2 v[44:45], v[42:43], off
	v_or_b32_e32 v44, 36, v30
	s_waitcnt vmcnt(15)
	v_mul_f32_e32 v42, v79, v79
	v_mul_f32_e32 v43, v81, v81
	v_ashrrev_i32_e32 v45, 31, v44
	v_fmac_f32_e32 v42, v78, v78
	v_fmac_f32_e32 v43, v80, v80
	v_lshlrev_b64 v[44:45], 15, v[44:45]
	v_add_f32_e32 v42, v42, v43
	v_bitop3_b32 v44, v44, -2, v94 bitop3:0xc8
	v_add_f32_e32 v31, v31, v42
	v_cvt_pk_bf16_f32 v42, v78, v79
	v_cvt_pk_bf16_f32 v43, v80, v81
	v_lshl_add_u64 v[44:45], s[0:1], 0, v[44:45]
	global_store_dwordx2 v[44:45], v[42:43], off
	s_waitcnt vmcnt(15)
	v_mul_f32_e32 v42, v19, v19
	v_mul_f32_e32 v43, v21, v21
	v_fmac_f32_e32 v42, v18, v18
	v_fmac_f32_e32 v43, v20, v20
	v_cvt_pk_bf16_f32 v18, v18, v19
	v_cvt_pk_bf16_f32 v19, v20, v21
	v_or_b32_e32 v20, 40, v30
	v_ashrrev_i32_e32 v21, 31, v20
	v_lshlrev_b64 v[20:21], 15, v[20:21]
	v_bitop3_b32 v20, v20, -2, v94 bitop3:0xc8
	v_lshl_add_u64 v[20:21], s[0:1], 0, v[20:21]
	global_store_dwordx2 v[20:21], v[18:19], off
	s_waitcnt vmcnt(15)
	v_mul_f32_e32 v18, v15, v15
	v_mul_f32_e32 v19, v17, v17
	v_fmac_f32_e32 v18, v14, v14
	v_fmac_f32_e32 v19, v16, v16
	v_cvt_pk_bf16_f32 v14, v14, v15
	v_cvt_pk_bf16_f32 v15, v16, v17
	v_or_b32_e32 v16, 44, v30
	v_ashrrev_i32_e32 v17, 31, v16
	v_lshlrev_b64 v[16:17], 15, v[16:17]
	v_bitop3_b32 v16, v16, -2, v94 bitop3:0xc8
	v_lshl_add_u64 v[16:17], s[0:1], 0, v[16:17]
	global_store_dwordx2 v[16:17], v[14:15], off
	v_or_b32_e32 v16, 48, v30
	v_add_f32_e32 v42, v42, v43
	s_waitcnt vmcnt(15)
	v_mul_f32_e32 v14, v23, v23
	v_mul_f32_e32 v15, v25, v25
	v_ashrrev_i32_e32 v17, 31, v16
	v_add_f32_e32 v31, v31, v42
	v_add_f32_e32 v18, v18, v19
	v_fmac_f32_e32 v14, v22, v22
	v_fmac_f32_e32 v15, v24, v24
	v_lshlrev_b64 v[16:17], 15, v[16:17]
	v_add_f32_e32 v18, v31, v18
	v_add_f32_e32 v14, v14, v15
	v_bitop3_b32 v16, v16, -2, v94 bitop3:0xc8
	v_add_f32_e32 v18, v18, v14
	v_cvt_pk_bf16_f32 v14, v22, v23
	v_cvt_pk_bf16_f32 v15, v24, v25
	v_lshl_add_u64 v[16:17], s[0:1], 0, v[16:17]
	global_store_dwordx2 v[16:17], v[14:15], off
	s_waitcnt vmcnt(15)
	v_mul_f32_e32 v14, v11, v11
	v_mul_f32_e32 v15, v13, v13
	v_fmac_f32_e32 v14, v10, v10
	v_fmac_f32_e32 v15, v12, v12
	v_add_f32_e32 v14, v14, v15
	s_waitcnt vmcnt(14)
	v_mul_f32_e32 v15, v7, v7
	v_mul_f32_e32 v16, v9, v9
	v_fmac_f32_e32 v15, v6, v6
	v_fmac_f32_e32 v16, v8, v8
	v_add_f32_e32 v14, v18, v14
	v_add_f32_e32 v15, v15, v16
	v_add_f32_e32 v14, v14, v15
	s_waitcnt vmcnt(13)
	v_mul_f32_e32 v15, v3, v3
	v_mul_f32_e32 v16, v5, v5
	v_fmac_f32_e32 v15, v2, v2
	v_fmac_f32_e32 v16, v4, v4
	v_add_f32_e32 v15, v15, v16
	v_add_f32_e32 v14, v14, v15
	v_cndmask_b32_e32 v15, v26, v36, vcc
	v_lshlrev_b32_e32 v15, 2, v15
	ds_bpermute_b32 v15, v15, v14
	v_cmp_lt_i32_e32 vcc, v37, v35
	v_cvt_pk_bf16_f32 v10, v10, v11
	v_cvt_pk_bf16_f32 v11, v12, v13
	v_or_b32_e32 v12, 52, v30
	s_waitcnt lgkmcnt(0)
	v_add_f32_e32 v14, v14, v15
	v_cndmask_b32_e32 v15, v26, v37, vcc
	v_lshlrev_b32_e32 v15, 2, v15
	v_ashrrev_i32_e32 v13, 31, v12
	ds_bpermute_b32 v15, v15, v14
	v_lshlrev_b64 v[12:13], 15, v[12:13]
	v_bitop3_b32 v12, v12, -2, v94 bitop3:0xc8
	v_lshl_add_u64 v[12:13], s[0:1], 0, v[12:13]
	v_cmp_lt_i32_e32 vcc, v38, v35
	global_store_dwordx2 v[12:13], v[10:11], off
	s_waitcnt lgkmcnt(0)
	v_add_f32_e32 v10, v14, v15
	v_cndmask_b32_e32 v11, v26, v38, vcc
	v_lshlrev_b32_e32 v11, 2, v11
	ds_bpermute_b32 v11, v11, v10
	v_cmp_lt_i32_e32 vcc, v39, v35
	v_cvt_pk_bf16_f32 v6, v6, v7
	v_cvt_pk_bf16_f32 v7, v8, v9
	v_or_b32_e32 v8, 56, v30
	s_waitcnt lgkmcnt(0)
	v_add_f32_e32 v10, v10, v11
	v_cndmask_b32_e32 v11, v26, v39, vcc
	v_lshlrev_b32_e32 v11, 2, v11
	v_ashrrev_i32_e32 v9, 31, v8
	ds_bpermute_b32 v11, v11, v10
	v_lshlrev_b64 v[8:9], 15, v[8:9]
	v_bitop3_b32 v8, v8, -2, v94 bitop3:0xc8
	v_lshl_add_u64 v[8:9], s[0:1], 0, v[8:9]
	v_cmp_lt_i32_e32 vcc, v40, v35
	global_store_dwordx2 v[8:9], v[6:7], off
	s_waitcnt lgkmcnt(0)
	v_add_f32_e32 v8, v10, v11
	v_cndmask_b32_e32 v6, v26, v40, vcc
	v_lshlrev_b32_e32 v6, 2, v6
	ds_bpermute_b32 v9, v6, v8
	v_cmp_lt_i32_e32 vcc, v41, v35
	v_cvt_pk_bf16_f32 v6, v2, v3
	v_cvt_pk_bf16_f32 v7, v4, v5
	v_cndmask_b32_e32 v3, v26, v41, vcc
	s_waitcnt lgkmcnt(0)
	v_add_f32_e32 v2, v8, v9
	v_lshlrev_b32_e32 v3, 2, v3
	v_or_b32_e32 v4, 60, v30
	ds_bpermute_b32 v3, v3, v2
	v_ashrrev_i32_e32 v5, 31, v4
	v_lshlrev_b64 v[4:5], 15, v[4:5]
	v_bitop3_b32 v4, v4, -2, v94 bitop3:0xc8
	v_lshl_add_u64 v[4:5], s[0:1], 0, v[4:5]
	global_store_dwordx2 v[4:5], v[6:7], off
	s_and_saveexec_b64 s[14:15], s[6:7]
	s_cbranch_execz .LBB0_174
	s_waitcnt lgkmcnt(0)
	v_add_f32_e32 v2, v2, v3
	global_store_dword v27, v2, s[4:5]
	s_branch .LBB0_174

; #define GAS __attribute__((address_space(1)))
; template <bool UNCOND> DI void witem_load(const WItem& d, WRegs& R, int lane) {
;     const int n4 = lane & 31, kh = lane >> 5;
;     const float* src = d.W + (size_t)(d.k0 + 2 * kh) * d.N + d.src_col0 + 4 * n4;
; #pragma unroll
;     for (int i = 0; i < 8; ++i) { R.a[i] = *(const GAS f32x4*)(src + (size_t)(4 * i) * d.N); R.b[i] = *(const GAS f32x4*)(src + (size_t)(4 * i + 1) * d.N); }
;     if (UNCOND) {
;         const float* gp = d.gain ? d.gain + d.k0 + 2 * kh : src;
; #pragma unroll
;         for (int i = 0; i < 8; ++i) R.gg[i] = *(const GAS f32x2g*)(gp + 4 * i);
;         if (!d.gain) {
; #pragma unroll
;             for (int i = 0; i < 8; ++i) R.gg[i] = (f32x2g){1.f, 1.f}; }
;     } else if (d.gain) {
; #pragma unroll
;         for (int i = 0; i < 8; ++i) R.gg[i] = *(const GAS f32x2g*)(d.gain + d.k0 + 4 * i + 2 * kh); }
;     ...
;     if (v0) witem_load<PIPE>(d0, R0, lane);
.LBB0_584:
	v_cndmask_b32_e64 v2, 0, 1, s[4:5]
	v_cmp_ne_u32_e64 s[0:1], 1, v2
	s_andn2_b64 vcc, exec, s[4:5]
	s_cbranch_vccnz .LBB0_587
	v_lshrrev_b32_e32 v2, 4, v0
	v_and_b32_e32 v66, 2, v2
	v_add_u32_e32 v2, s14, v66
	v_mad_i64_i32 v[2:3], s[4:5], s16, v2, 0
	v_lshl_add_u64 v[2:3], v[2:3], 2, s[8:9]
	s_ashr_i32 s19, s18, 31
	v_lshlrev_b32_e32 v4, 4, v0
	s_ashr_i32 s17, s16, 31
	v_lshl_add_u64 v[2:3], s[18:19], 2, v[2:3]
	v_and_b32_e32 v4, 0x1f0, v4
	v_mov_b32_e32 v5, 0
	v_lshl_add_u64 v[2:3], v[2:3], 0, v[4:5]
	s_lshl_b64 s[4:5], s[16:17], 2
	v_lshl_add_u64 v[10:11], v[2:3], 0, s[4:5]
	global_load_dwordx4 v[6:9], v[2:3], off nt
	s_nop 0
	global_load_dwordx4 v[2:5], v[10:11], off nt
	v_mad_i64_i32 v[10:11], s[6:7], s16, 12, v[10:11]
	v_lshl_add_u64 v[18:19], v[10:11], 0, s[4:5]
	global_load_dwordx4 v[14:17], v[10:11], off nt
	s_nop 0
	global_load_dwordx4 v[10:13], v[18:19], off nt
	v_mad_i64_i32 v[18:19], s[6:7], s16, 12, v[18:19]
	s_waitcnt vmcnt(0)
	v_lshl_add_u64 v[26:27], v[18:19], 0, s[4:5]
	global_load_dwordx4 v[22:25], v[18:19], off nt
	s_nop 0
	global_load_dwordx4 v[18:21], v[26:27], off nt
	v_mad_i64_i32 v[26:27], s[6:7], s16, 12, v[26:27]
	v_lshl_add_u64 v[34:35], v[26:27], 0, s[4:5]
	global_load_dwordx4 v[30:33], v[26:27], off nt
	s_nop 0
	global_load_dwordx4 v[26:29], v[34:35], off nt
	v_mad_i64_i32 v[34:35], s[6:7], s16, 12, v[34:35]
	v_lshl_add_u64 v[42:43], v[34:35], 0, s[4:5]
	global_load_dwordx4 v[38:41], v[34:35], off nt
	s_cmp_eq_u64 s[10:11], 0
	global_load_dwordx4 v[34:37], v[42:43], off nt
	v_mad_i64_i32 v[42:43], s[6:7], s16, 12, v[42:43]
	v_lshl_add_u64 v[50:51], v[42:43], 0, s[4:5]
	global_load_dwordx4 v[46:49], v[42:43], off nt
	s_nop 0
	global_load_dwordx4 v[42:45], v[50:51], off nt
	v_mad_i64_i32 v[50:51], s[6:7], s16, 12, v[50:51]
	v_lshl_add_u64 v[58:59], v[50:51], 0, s[4:5]
	global_load_dwordx4 v[54:57], v[50:51], off nt
	s_nop 0
	global_load_dwordx4 v[50:53], v[58:59], off nt
	v_mad_i64_i32 v[58:59], s[6:7], s16, 12, v[58:59]
	global_load_dwordx4 v[62:65], v[58:59], off nt
	v_lshl_add_u64 v[58:59], v[58:59], 0, s[4:5]
	global_load_dwordx4 v[58:61], v[58:59], off nt
	s_cbranch_scc1 .LBB0_588
	s_ashr_i32 s15, s14, 31
	s_lshl_b64 s[4:5], s[14:15], 2
	s_add_u32 s4, s10, s4
	s_addc_u32 s5, s11, s5
	v_lshlrev_b32_e32 v66, 2, v66
	global_load_dwordx2 v[130:131], v66, s[4:5]
	global_load_dwordx2 v[132:133], v66, s[4:5] offset:16
	global_load_dwordx2 v[134:135], v66, s[4:5] offset:32
	global_load_dwordx2 v[136:137], v66, s[4:5] offset:48
	global_load_dwordx2 v[138:139], v66, s[4:5] offset:64
	global_load_dwordx2 v[140:141], v66, s[4:5] offset:80
	global_load_dwordx2 v[142:143], v66, s[4:5] offset:96
	global_load_dwordx2 v[144:145], v66, s[4:5] offset:112
	s_and_b64 vcc, exec, s[0:1]
	s_cbranch_vccz .LBB0_589
	s_branch .LBB0_727

; #define GAS __attribute__((address_space(1)))
; template <bool UNCOND> DI void witem_load(const WItem& d, WRegs& R, int lane) {
;     const int n4 = lane & 31, kh = lane >> 5;
;     const float* src = d.W + (size_t)(d.k0 + 2 * kh) * d.N + d.src_col0 + 4 * n4;
; #pragma unroll
;     for (int i = 0; i < 8; ++i) { R.a[i] = *(const GAS f32x4*)(src + (size_t)(4 * i) * d.N); R.b[i] = *(const GAS f32x4*)(src + (size_t)(4 * i + 1) * d.N); }
;     if (UNCOND) {
;         const float* gp = d.gain ? d.gain + d.k0 + 2 * kh : src;
; #pragma unroll
;         for (int i = 0; i < 8; ++i) R.gg[i] = *(const GAS f32x2g*)(gp + 4 * i);
;         if (!d.gain) {
; #pragma unroll
;             for (int i = 0; i < 8; ++i) R.gg[i] = (f32x2g){1.f, 1.f}; }
;     } else if (d.gain) {
; #pragma unroll
;         for (int i = 0; i < 8; ++i) R.gg[i] = *(const GAS f32x2g*)(d.gain + d.k0 + 4 * i + 2 * kh); }
;     else {
; #pragma unroll
;         for (int i = 0; i < 8; ++i) R.gg[i] = (f32x2g){1.f, 1.f}; }
;     ...
;         const bool v1 = it + ST < wend && witem_decode<EARLY>(P, it + ST, d1);
;         if (PIPE) { if (!v1) d1 = d0; witem_load<true>(d1, R1, lane); } else if (v1) witem_load<false>(d1, R1, lane);
.LBB0_611:
	v_cndmask_b32_e64 v150, 0, 1, s[4:5]
	v_cmp_ne_u32_e64 s[0:1], 1, v150
	s_andn2_b64 vcc, exec, s[4:5]
	s_cbranch_vccnz .LBB0_615
	s_waitcnt vmcnt(23)
	v_add_u32_e32 v66, s36, v146
	v_mad_i64_i32 v[66:67], s[4:5], s38, v66, 0
	v_lshl_add_u64 v[66:67], v[66:67], 2, s[30:31]
	s_ashr_i32 s43, s42, 31
	s_ashr_i32 s39, s38, 31
	v_lshl_add_u64 v[66:67], s[42:43], 2, v[66:67]
	v_lshlrev_b32_e32 v150, 2, v148
	v_lshl_add_u64 v[66:67], v[66:67], 0, v[150:151]
	s_lshl_b64 s[4:5], s[38:39], 2
	s_waitcnt vmcnt(21)
	v_lshl_add_u64 v[70:71], v[66:67], 0, s[4:5]
	global_load_dwordx4 v[66:69], v[66:67], off nt
	s_nop 0
	global_load_dwordx4 v[74:77], v[70:71], off nt
	v_mad_i64_i32 v[70:71], s[6:7], s38, 12, v[70:71]
	s_waitcnt vmcnt(21)
	v_lshl_add_u64 v[78:79], v[70:71], 0, s[4:5]
	global_load_dwordx4 v[70:73], v[70:71], off nt
	s_nop 0
	global_load_dwordx4 v[82:85], v[78:79], off nt
	v_mad_i64_i32 v[78:79], s[6:7], s38, 12, v[78:79]
	s_waitcnt vmcnt(21)
	v_lshl_add_u64 v[86:87], v[78:79], 0, s[4:5]
	global_load_dwordx4 v[78:81], v[78:79], off nt
	s_nop 0
	global_load_dwordx4 v[90:93], v[86:87], off nt
	v_mad_i64_i32 v[86:87], s[6:7], s38, 12, v[86:87]
	s_waitcnt vmcnt(21)
	v_lshl_add_u64 v[94:95], v[86:87], 0, s[4:5]
	s_waitcnt vmcnt(19)
	v_mad_i64_i32 v[102:103], s[6:7], s38, 12, v[94:95]
	global_load_dwordx4 v[86:89], v[86:87], off nt
	s_nop 0
	global_load_dwordx4 v[98:101], v[94:95], off nt
	s_cmp_eq_u64 s[34:35], 0
	global_load_dwordx4 v[94:97], v[102:103], off nt
	v_lshl_add_u64 v[102:103], v[102:103], 0, s[4:5]
	s_waitcnt vmcnt(20)
	v_mad_i64_i32 v[110:111], s[6:7], s38, 12, v[102:103]
	global_load_dwordx4 v[106:109], v[102:103], off nt
	s_nop 0
	global_load_dwordx4 v[102:105], v[110:111], off nt
	v_lshl_add_u64 v[110:111], v[110:111], 0, s[4:5]
	s_waitcnt vmcnt(20)
	v_mad_i64_i32 v[118:119], s[6:7], s38, 12, v[110:111]
	global_load_dwordx4 v[114:117], v[110:111], off nt
	s_nop 0
	global_load_dwordx4 v[110:113], v[118:119], off nt
	v_lshl_add_u64 v[118:119], v[118:119], 0, s[4:5]
	s_waitcnt vmcnt(21)
	v_mad_i64_i32 v[126:127], s[6:7], s38, 12, v[118:119]
	global_load_dwordx4 v[122:125], v[118:119], off nt
	s_nop 0
	global_load_dwordx4 v[118:121], v[126:127], off nt
	v_lshl_add_u64 v[126:127], v[126:127], 0, s[4:5]
	global_load_dwordx4 v[126:129], v[126:127], off nt
	s_cbranch_scc1 .LBB0_614
	s_ashr_i32 s37, s36, 31
	s_lshl_b64 s[4:5], s[36:37], 2
	s_add_u32 s4, s34, s4
	s_addc_u32 s5, s35, s5
	v_lshlrev_b32_e32 v150, 2, v146
	global_load_dwordx2 v[152:153], v150, s[4:5]
	global_load_dwordx2 v[154:155], v150, s[4:5] offset:16
	global_load_dwordx2 v[156:157], v150, s[4:5] offset:32
	global_load_dwordx2 v[158:159], v150, s[4:5] offset:48
	global_load_dwordx2 v[160:161], v150, s[4:5] offset:64
	global_load_dwordx2 v[162:163], v150, s[4:5] offset:80
	global_load_dwordx2 v[164:165], v150, s[4:5] offset:96
	global_load_dwordx2 v[166:167], v150, s[4:5] offset:112
	s_branch .LBB0_615

; #define GAS __attribute__((address_space(1)))
; template <bool UNCOND> DI void witem_load(const WItem& d, WRegs& R, int lane) {
;     const int n4 = lane & 31, kh = lane >> 5;
;     const float* src = d.W + (size_t)(d.k0 + 2 * kh) * d.N + d.src_col0 + 4 * n4;
; #pragma unroll
;     for (int i = 0; i < 8; ++i) { R.a[i] = *(const GAS f32x4*)(src + (size_t)(4 * i) * d.N); R.b[i] = *(const GAS f32x4*)(src + (size_t)(4 * i + 1) * d.N); }
;     if (UNCOND) {
;         const float* gp = d.gain ? d.gain + d.k0 + 2 * kh : src;
; #pragma unroll
;         for (int i = 0; i < 8; ++i) R.gg[i] = *(const GAS f32x2g*)(gp + 4 * i);
;         if (!d.gain) {
; #pragma unroll
;             for (int i = 0; i < 8; ++i) R.gg[i] = (f32x2g){1.f, 1.f}; }
;     } else if (d.gain) {
; #pragma unroll
;         for (int i = 0; i < 8; ++i) R.gg[i] = *(const GAS f32x2g*)(d.gain + d.k0 + 4 * i + 2 * kh); }
;     else {
; #pragma unroll
;         for (int i = 0; i < 8; ++i) R.gg[i] = (f32x2g){1.f, 1.f}; }
;     ...
;         v0 = it + 2 * ST < wend && witem_decode<EARLY>(P, it + 2 * ST, d0);
;         if (PIPE) { if (!v0) d0 = d1; witem_load<true>(d0, R0, lane); } else if (v0) witem_load<false>(d0, R0, lane);
.LBB0_679:
	s_andn2_b64 vcc, exec, s[0:1]
	s_cbranch_vccnz .LBB0_683
	v_add_u32_e32 v2, s14, v146
	v_mad_i64_i32 v[2:3], s[0:1], s16, v2, 0
	v_lshl_add_u64 v[2:3], v[2:3], 2, s[8:9]
	s_ashr_i32 s19, s18, 31
	s_ashr_i32 s17, s16, 31
	v_lshl_add_u64 v[2:3], s[18:19], 2, v[2:3]
	v_lshlrev_b32_e32 v150, 2, v148
	v_lshl_add_u64 v[2:3], v[2:3], 0, v[150:151]
	s_lshl_b64 s[0:1], s[16:17], 2
	v_lshl_add_u64 v[10:11], v[2:3], 0, s[0:1]
	global_load_dwordx4 v[6:9], v[2:3], off nt
	s_nop 0
	global_load_dwordx4 v[2:5], v[10:11], off nt
	v_mad_i64_i32 v[10:11], s[4:5], s16, 12, v[10:11]
	v_lshl_add_u64 v[18:19], v[10:11], 0, s[0:1]
	global_load_dwordx4 v[14:17], v[10:11], off nt
	s_nop 0
	global_load_dwordx4 v[10:13], v[18:19], off nt
	v_mad_i64_i32 v[18:19], s[4:5], s16, 12, v[18:19]
	v_lshl_add_u64 v[26:27], v[18:19], 0, s[0:1]
	global_load_dwordx4 v[22:25], v[18:19], off nt
	s_nop 0
	global_load_dwordx4 v[18:21], v[26:27], off nt
	v_mad_i64_i32 v[26:27], s[4:5], s16, 12, v[26:27]
	v_lshl_add_u64 v[34:35], v[26:27], 0, s[0:1]
	global_load_dwordx4 v[30:33], v[26:27], off nt
	s_nop 0
	global_load_dwordx4 v[26:29], v[34:35], off nt
	v_mad_i64_i32 v[34:35], s[4:5], s16, 12, v[34:35]
	v_lshl_add_u64 v[42:43], v[34:35], 0, s[0:1]
	global_load_dwordx4 v[38:41], v[34:35], off nt
	s_cmp_eq_u64 s[10:11], 0
	global_load_dwordx4 v[34:37], v[42:43], off nt
	v_mad_i64_i32 v[42:43], s[4:5], s16, 12, v[42:43]
	v_lshl_add_u64 v[50:51], v[42:43], 0, s[0:1]
	global_load_dwordx4 v[46:49], v[42:43], off nt
	s_nop 0
	global_load_dwordx4 v[42:45], v[50:51], off nt
	v_mad_i64_i32 v[50:51], s[4:5], s16, 12, v[50:51]
	v_lshl_add_u64 v[58:59], v[50:51], 0, s[0:1]
	global_load_dwordx4 v[54:57], v[50:51], off nt
	s_nop 0
	global_load_dwordx4 v[50:53], v[58:59], off nt
	v_mad_i64_i32 v[58:59], s[4:5], s16, 12, v[58:59]
	global_load_dwordx4 v[62:65], v[58:59], off nt
	v_lshl_add_u64 v[58:59], v[58:59], 0, s[0:1]
	global_load_dwordx4 v[58:61], v[58:59], off nt
	s_cbranch_scc1 .LBB0_682
	s_ashr_i32 s15, s14, 31
	s_lshl_b64 s[0:1], s[14:15], 2
	s_add_u32 s0, s10, s0
	s_addc_u32 s1, s11, s1
	v_lshlrev_b32_e32 v144, 2, v146
	global_load_dwordx2 v[130:131], v144, s[0:1]
	global_load_dwordx2 v[132:133], v144, s[0:1] offset:16
	global_load_dwordx2 v[134:135], v144, s[0:1] offset:32
	global_load_dwordx2 v[136:137], v144, s[0:1] offset:48
	global_load_dwordx2 v[138:139], v144, s[0:1] offset:64
	global_load_dwordx2 v[140:141], v144, s[0:1] offset:80
	global_load_dwordx2 v[142:143], v144, s[0:1] offset:96
	s_nop 0
	global_load_dwordx2 v[144:145], v144, s[0:1] offset:112
	s_branch .LBB0_683
